# baseline (speedup 1.0000x reference)
_Z11prep_kernelPKfS0_S0_PDF16_PfPiS0_S1_:
	s_cmpk_lt_u32 s2, 0xc1
	s_mov_b64 s[4:5], -1
	s_cbranch_scc0 .LBB0_51
	s_cmpk_lg_i32 s2, 0xc0
	s_cbranch_scc0 .LBB0_11
	s_cmp_gt_u32 s2, 63
	s_cbranch_scc0 .LBB0_8
	s_load_dwordx4 s[4:7], s[0:1], 0x0
	s_load_dwordx2 s[28:29], s[0:1], 0x20
	s_sub_u32 s3, s2, 64
	v_readfirstlane_b32 s23, v0
	v_and_b32_e32 v1, 63, v0
	v_lshlrev_b32_e32 v100, 4, v1
	s_lshr_b32 s23, s23, 6
	s_lshr_b32 s27, s3, 1
	s_and_b32 s30, s3, 1
	s_lshl_b32 s8, s27, 12
	s_lshl_b32 s9, s23, 6
	s_add_u32 s8, s8, s9
	s_lshl_b32 s10, s23, 15
	s_lshl_b32 s9, s30, 10
	s_add_u32 s10, s10, s9
	s_waitcnt lgkmcnt(0)
	s_add_u32 s20, s4, s8
	s_addc_u32 s21, s5, 0
	s_add_u32 s24, s6, s10
	s_addc_u32 s25, s7, 0
	global_load_dwordx4 v[34:37], v100, s[24:25]
	global_load_dwordx4 v[38:41], v100, s[24:25] offset:2048
	s_add_u32 s24, s24, 0x1000
	s_addc_u32 s25, s25, 0
	s_load_dwordx8 s[32:39], s[20:21], 0x0
	s_load_dwordx8 s[40:47], s[20:21], 0x200
	s_load_dwordx8 s[48:55], s[20:21], 0x400
	s_load_dwordx8 s[56:63], s[20:21], 0x600
	global_load_dwordx4 v[42:45], v100, s[24:25]
	global_load_dwordx4 v[46:49], v100, s[24:25] offset:2048
	s_add_u32 s24, s24, 0x1000
	s_addc_u32 s25, s25, 0
	s_load_dwordx8 s[64:71], s[20:21], 0x20
	s_load_dwordx8 s[72:79], s[20:21], 0x220
	s_load_dwordx8 s[80:87], s[20:21], 0x420
	s_load_dwordx8 s[88:95], s[20:21], 0x620
	global_load_dwordx4 v[50:53], v100, s[24:25]
	global_load_dwordx4 v[54:57], v100, s[24:25] offset:2048
	s_add_u32 s24, s24, 0x1000
	s_addc_u32 s25, s25, 0
	global_load_dwordx4 v[58:61], v100, s[24:25]
	global_load_dwordx4 v[62:65], v100, s[24:25] offset:2048
	s_add_u32 s24, s24, 0x1000
	s_addc_u32 s25, s25, 0
	global_load_dwordx4 v[66:69], v100, s[24:25]
	global_load_dwordx4 v[70:73], v100, s[24:25] offset:2048
	s_add_u32 s24, s24, 0x1000
	s_addc_u32 s25, s25, 0
	global_load_dwordx4 v[74:77], v100, s[24:25]
	global_load_dwordx4 v[78:81], v100, s[24:25] offset:2048
	s_add_u32 s24, s24, 0x1000
	s_addc_u32 s25, s25, 0
	global_load_dwordx4 v[82:85], v100, s[24:25]
	global_load_dwordx4 v[86:89], v100, s[24:25] offset:2048
	s_add_u32 s24, s24, 0x1000
	s_addc_u32 s25, s25, 0
	global_load_dwordx4 v[90:93], v100, s[24:25]
	global_load_dwordx4 v[94:97], v100, s[24:25] offset:2048
	v_mov_b64_e32 v[2:3], 0
	v_mov_b64_e32 v[4:5], 0
	v_mov_b64_e32 v[6:7], 0
	v_mov_b64_e32 v[8:9], 0
	v_mov_b64_e32 v[10:11], 0
	v_mov_b64_e32 v[12:13], 0
	v_mov_b64_e32 v[14:15], 0
	v_mov_b64_e32 v[16:17], 0
	v_mov_b64_e32 v[18:19], 0
	v_mov_b64_e32 v[20:21], 0
	v_mov_b64_e32 v[22:23], 0
	v_mov_b64_e32 v[24:25], 0
	v_mov_b64_e32 v[26:27], 0
	v_mov_b64_e32 v[28:29], 0
	v_mov_b64_e32 v[30:31], 0
	v_mov_b64_e32 v[32:33], 0
	s_waitcnt lgkmcnt(0)
	s_waitcnt vmcnt(15)
	v_pk_fma_f32 v[2:3], s[32:33], v[34:35], v[2:3] op_sel_hi:[0,1,1]
	v_pk_fma_f32 v[4:5], s[32:33], v[36:37], v[4:5] op_sel_hi:[0,1,1]
	v_pk_fma_f32 v[6:7], s[40:41], v[34:35], v[6:7] op_sel_hi:[0,1,1]
	v_pk_fma_f32 v[8:9], s[40:41], v[36:37], v[8:9] op_sel_hi:[0,1,1]
	v_pk_fma_f32 v[10:11], s[48:49], v[34:35], v[10:11] op_sel_hi:[0,1,1]
	v_pk_fma_f32 v[12:13], s[48:49], v[36:37], v[12:13] op_sel_hi:[0,1,1]
	v_pk_fma_f32 v[14:15], s[56:57], v[34:35], v[14:15] op_sel_hi:[0,1,1]
	v_pk_fma_f32 v[16:17], s[56:57], v[36:37], v[16:17] op_sel_hi:[0,1,1]
	s_waitcnt vmcnt(14)
	v_pk_fma_f32 v[2:3], s[32:33], v[38:39], v[2:3] op_sel:[1,0,0]
	v_pk_fma_f32 v[4:5], s[32:33], v[40:41], v[4:5] op_sel:[1,0,0]
	v_pk_fma_f32 v[6:7], s[40:41], v[38:39], v[6:7] op_sel:[1,0,0]
	v_pk_fma_f32 v[8:9], s[40:41], v[40:41], v[8:9] op_sel:[1,0,0]
	v_pk_fma_f32 v[10:11], s[48:49], v[38:39], v[10:11] op_sel:[1,0,0]
	v_pk_fma_f32 v[12:13], s[48:49], v[40:41], v[12:13] op_sel:[1,0,0]
	v_pk_fma_f32 v[14:15], s[56:57], v[38:39], v[14:15] op_sel:[1,0,0]
	v_pk_fma_f32 v[16:17], s[56:57], v[40:41], v[16:17] op_sel:[1,0,0]
	s_waitcnt vmcnt(13)
	v_pk_fma_f32 v[2:3], s[34:35], v[42:43], v[2:3] op_sel_hi:[0,1,1]
	v_pk_fma_f32 v[4:5], s[34:35], v[44:45], v[4:5] op_sel_hi:[0,1,1]
	v_pk_fma_f32 v[6:7], s[42:43], v[42:43], v[6:7] op_sel_hi:[0,1,1]
	v_pk_fma_f32 v[8:9], s[42:43], v[44:45], v[8:9] op_sel_hi:[0,1,1]
	v_pk_fma_f32 v[10:11], s[50:51], v[42:43], v[10:11] op_sel_hi:[0,1,1]
	v_pk_fma_f32 v[12:13], s[50:51], v[44:45], v[12:13] op_sel_hi:[0,1,1]
	v_pk_fma_f32 v[14:15], s[58:59], v[42:43], v[14:15] op_sel_hi:[0,1,1]
	v_pk_fma_f32 v[16:17], s[58:59], v[44:45], v[16:17] op_sel_hi:[0,1,1]
	s_waitcnt vmcnt(12)
	v_pk_fma_f32 v[2:3], s[34:35], v[46:47], v[2:3] op_sel:[1,0,0]
	v_pk_fma_f32 v[4:5], s[34:35], v[48:49], v[4:5] op_sel:[1,0,0]
	v_pk_fma_f32 v[6:7], s[42:43], v[46:47], v[6:7] op_sel:[1,0,0]
	v_pk_fma_f32 v[8:9], s[42:43], v[48:49], v[8:9] op_sel:[1,0,0]
	v_pk_fma_f32 v[10:11], s[50:51], v[46:47], v[10:11] op_sel:[1,0,0]
	v_pk_fma_f32 v[12:13], s[50:51], v[48:49], v[12:13] op_sel:[1,0,0]
	v_pk_fma_f32 v[14:15], s[58:59], v[46:47], v[14:15] op_sel:[1,0,0]
	v_pk_fma_f32 v[16:17], s[58:59], v[48:49], v[16:17] op_sel:[1,0,0]
	s_waitcnt vmcnt(11)
	v_pk_fma_f32 v[2:3], s[36:37], v[50:51], v[2:3] op_sel_hi:[0,1,1]
	v_pk_fma_f32 v[4:5], s[36:37], v[52:53], v[4:5] op_sel_hi:[0,1,1]
	v_pk_fma_f32 v[6:7], s[44:45], v[50:51], v[6:7] op_sel_hi:[0,1,1]
	v_pk_fma_f32 v[8:9], s[44:45], v[52:53], v[8:9] op_sel_hi:[0,1,1]
	v_pk_fma_f32 v[10:11], s[52:53], v[50:51], v[10:11] op_sel_hi:[0,1,1]
	v_pk_fma_f32 v[12:13], s[52:53], v[52:53], v[12:13] op_sel_hi:[0,1,1]
	v_pk_fma_f32 v[14:15], s[60:61], v[50:51], v[14:15] op_sel_hi:[0,1,1]
	v_pk_fma_f32 v[16:17], s[60:61], v[52:53], v[16:17] op_sel_hi:[0,1,1]
	s_waitcnt vmcnt(10)
	v_pk_fma_f32 v[2:3], s[36:37], v[54:55], v[2:3] op_sel:[1,0,0]
	v_pk_fma_f32 v[4:5], s[36:37], v[56:57], v[4:5] op_sel:[1,0,0]
	v_pk_fma_f32 v[6:7], s[44:45], v[54:55], v[6:7] op_sel:[1,0,0]
	v_pk_fma_f32 v[8:9], s[44:45], v[56:57], v[8:9] op_sel:[1,0,0]
	v_pk_fma_f32 v[10:11], s[52:53], v[54:55], v[10:11] op_sel:[1,0,0]
	v_pk_fma_f32 v[12:13], s[52:53], v[56:57], v[12:13] op_sel:[1,0,0]
	v_pk_fma_f32 v[14:15], s[60:61], v[54:55], v[14:15] op_sel:[1,0,0]
	v_pk_fma_f32 v[16:17], s[60:61], v[56:57], v[16:17] op_sel:[1,0,0]
	s_waitcnt vmcnt(9)
	v_pk_fma_f32 v[2:3], s[38:39], v[58:59], v[2:3] op_sel_hi:[0,1,1]
	v_pk_fma_f32 v[4:5], s[38:39], v[60:61], v[4:5] op_sel_hi:[0,1,1]
	v_pk_fma_f32 v[6:7], s[46:47], v[58:59], v[6:7] op_sel_hi:[0,1,1]
	v_pk_fma_f32 v[8:9], s[46:47], v[60:61], v[8:9] op_sel_hi:[0,1,1]
	v_pk_fma_f32 v[10:11], s[54:55], v[58:59], v[10:11] op_sel_hi:[0,1,1]
	v_pk_fma_f32 v[12:13], s[54:55], v[60:61], v[12:13] op_sel_hi:[0,1,1]
	v_pk_fma_f32 v[14:15], s[62:63], v[58:59], v[14:15] op_sel_hi:[0,1,1]
	v_pk_fma_f32 v[16:17], s[62:63], v[60:61], v[16:17] op_sel_hi:[0,1,1]
	s_waitcnt vmcnt(8)
	v_pk_fma_f32 v[2:3], s[38:39], v[62:63], v[2:3] op_sel:[1,0,0]
	v_pk_fma_f32 v[4:5], s[38:39], v[64:65], v[4:5] op_sel:[1,0,0]
	v_pk_fma_f32 v[6:7], s[46:47], v[62:63], v[6:7] op_sel:[1,0,0]
	v_pk_fma_f32 v[8:9], s[46:47], v[64:65], v[8:9] op_sel:[1,0,0]
	v_pk_fma_f32 v[10:11], s[54:55], v[62:63], v[10:11] op_sel:[1,0,0]
	v_pk_fma_f32 v[12:13], s[54:55], v[64:65], v[12:13] op_sel:[1,0,0]
	v_pk_fma_f32 v[14:15], s[62:63], v[62:63], v[14:15] op_sel:[1,0,0]
	v_pk_fma_f32 v[16:17], s[62:63], v[64:65], v[16:17] op_sel:[1,0,0]
	s_load_dwordx8 s[32:39], s[20:21], 0x800
	s_load_dwordx8 s[40:47], s[20:21], 0xa00
	s_load_dwordx8 s[48:55], s[20:21], 0xc00
	s_load_dwordx8 s[56:63], s[20:21], 0xe00
	s_waitcnt vmcnt(7)
	v_pk_fma_f32 v[2:3], s[64:65], v[66:67], v[2:3] op_sel_hi:[0,1,1]
	v_pk_fma_f32 v[4:5], s[64:65], v[68:69], v[4:5] op_sel_hi:[0,1,1]
	v_pk_fma_f32 v[6:7], s[72:73], v[66:67], v[6:7] op_sel_hi:[0,1,1]
	v_pk_fma_f32 v[8:9], s[72:73], v[68:69], v[8:9] op_sel_hi:[0,1,1]
	v_pk_fma_f32 v[10:11], s[80:81], v[66:67], v[10:11] op_sel_hi:[0,1,1]
	v_pk_fma_f32 v[12:13], s[80:81], v[68:69], v[12:13] op_sel_hi:[0,1,1]
	v_pk_fma_f32 v[14:15], s[88:89], v[66:67], v[14:15] op_sel_hi:[0,1,1]
	v_pk_fma_f32 v[16:17], s[88:89], v[68:69], v[16:17] op_sel_hi:[0,1,1]
	s_waitcnt vmcnt(6)
	v_pk_fma_f32 v[2:3], s[64:65], v[70:71], v[2:3] op_sel:[1,0,0]
	v_pk_fma_f32 v[4:5], s[64:65], v[72:73], v[4:5] op_sel:[1,0,0]
	v_pk_fma_f32 v[6:7], s[72:73], v[70:71], v[6:7] op_sel:[1,0,0]
	v_pk_fma_f32 v[8:9], s[72:73], v[72:73], v[8:9] op_sel:[1,0,0]
	v_pk_fma_f32 v[10:11], s[80:81], v[70:71], v[10:11] op_sel:[1,0,0]
	v_pk_fma_f32 v[12:13], s[80:81], v[72:73], v[12:13] op_sel:[1,0,0]
	v_pk_fma_f32 v[14:15], s[88:89], v[70:71], v[14:15] op_sel:[1,0,0]
	v_pk_fma_f32 v[16:17], s[88:89], v[72:73], v[16:17] op_sel:[1,0,0]
	s_waitcnt vmcnt(5)
	v_pk_fma_f32 v[2:3], s[66:67], v[74:75], v[2:3] op_sel_hi:[0,1,1]
	v_pk_fma_f32 v[4:5], s[66:67], v[76:77], v[4:5] op_sel_hi:[0,1,1]
	v_pk_fma_f32 v[6:7], s[74:75], v[74:75], v[6:7] op_sel_hi:[0,1,1]
	v_pk_fma_f32 v[8:9], s[74:75], v[76:77], v[8:9] op_sel_hi:[0,1,1]
	v_pk_fma_f32 v[10:11], s[82:83], v[74:75], v[10:11] op_sel_hi:[0,1,1]
	v_pk_fma_f32 v[12:13], s[82:83], v[76:77], v[12:13] op_sel_hi:[0,1,1]
	v_pk_fma_f32 v[14:15], s[90:91], v[74:75], v[14:15] op_sel_hi:[0,1,1]
	v_pk_fma_f32 v[16:17], s[90:91], v[76:77], v[16:17] op_sel_hi:[0,1,1]
	s_waitcnt vmcnt(4)
	v_pk_fma_f32 v[2:3], s[66:67], v[78:79], v[2:3] op_sel:[1,0,0]
	v_pk_fma_f32 v[4:5], s[66:67], v[80:81], v[4:5] op_sel:[1,0,0]
	v_pk_fma_f32 v[6:7], s[74:75], v[78:79], v[6:7] op_sel:[1,0,0]
	v_pk_fma_f32 v[8:9], s[74:75], v[80:81], v[8:9] op_sel:[1,0,0]
	v_pk_fma_f32 v[10:11], s[82:83], v[78:79], v[10:11] op_sel:[1,0,0]
	v_pk_fma_f32 v[12:13], s[82:83], v[80:81], v[12:13] op_sel:[1,0,0]
	v_pk_fma_f32 v[14:15], s[90:91], v[78:79], v[14:15] op_sel:[1,0,0]
	v_pk_fma_f32 v[16:17], s[90:91], v[80:81], v[16:17] op_sel:[1,0,0]
	s_waitcnt vmcnt(3)
	v_pk_fma_f32 v[2:3], s[68:69], v[82:83], v[2:3] op_sel_hi:[0,1,1]
	v_pk_fma_f32 v[4:5], s[68:69], v[84:85], v[4:5] op_sel_hi:[0,1,1]
	v_pk_fma_f32 v[6:7], s[76:77], v[82:83], v[6:7] op_sel_hi:[0,1,1]
	v_pk_fma_f32 v[8:9], s[76:77], v[84:85], v[8:9] op_sel_hi:[0,1,1]
	v_pk_fma_f32 v[10:11], s[84:85], v[82:83], v[10:11] op_sel_hi:[0,1,1]
	v_pk_fma_f32 v[12:13], s[84:85], v[84:85], v[12:13] op_sel_hi:[0,1,1]
	v_pk_fma_f32 v[14:15], s[92:93], v[82:83], v[14:15] op_sel_hi:[0,1,1]
	v_pk_fma_f32 v[16:17], s[92:93], v[84:85], v[16:17] op_sel_hi:[0,1,1]
	s_waitcnt vmcnt(2)
	v_pk_fma_f32 v[2:3], s[68:69], v[86:87], v[2:3] op_sel:[1,0,0]
	v_pk_fma_f32 v[4:5], s[68:69], v[88:89], v[4:5] op_sel:[1,0,0]
	v_pk_fma_f32 v[6:7], s[76:77], v[86:87], v[6:7] op_sel:[1,0,0]
	v_pk_fma_f32 v[8:9], s[76:77], v[88:89], v[8:9] op_sel:[1,0,0]
	v_pk_fma_f32 v[10:11], s[84:85], v[86:87], v[10:11] op_sel:[1,0,0]
	v_pk_fma_f32 v[12:13], s[84:85], v[88:89], v[12:13] op_sel:[1,0,0]
	v_pk_fma_f32 v[14:15], s[92:93], v[86:87], v[14:15] op_sel:[1,0,0]
	v_pk_fma_f32 v[16:17], s[92:93], v[88:89], v[16:17] op_sel:[1,0,0]
	s_waitcnt vmcnt(1)
	v_pk_fma_f32 v[2:3], s[70:71], v[90:91], v[2:3] op_sel_hi:[0,1,1]
	v_pk_fma_f32 v[4:5], s[70:71], v[92:93], v[4:5] op_sel_hi:[0,1,1]
	v_pk_fma_f32 v[6:7], s[78:79], v[90:91], v[6:7] op_sel_hi:[0,1,1]
	v_pk_fma_f32 v[8:9], s[78:79], v[92:93], v[8:9] op_sel_hi:[0,1,1]
	v_pk_fma_f32 v[10:11], s[86:87], v[90:91], v[10:11] op_sel_hi:[0,1,1]
	v_pk_fma_f32 v[12:13], s[86:87], v[92:93], v[12:13] op_sel_hi:[0,1,1]
	v_pk_fma_f32 v[14:15], s[94:95], v[90:91], v[14:15] op_sel_hi:[0,1,1]
	v_pk_fma_f32 v[16:17], s[94:95], v[92:93], v[16:17] op_sel_hi:[0,1,1]
	s_waitcnt vmcnt(0)
	v_pk_fma_f32 v[2:3], s[70:71], v[94:95], v[2:3] op_sel:[1,0,0]
	v_pk_fma_f32 v[4:5], s[70:71], v[96:97], v[4:5] op_sel:[1,0,0]
	v_pk_fma_f32 v[6:7], s[78:79], v[94:95], v[6:7] op_sel:[1,0,0]
	v_pk_fma_f32 v[8:9], s[78:79], v[96:97], v[8:9] op_sel:[1,0,0]
	v_pk_fma_f32 v[10:11], s[86:87], v[94:95], v[10:11] op_sel:[1,0,0]
	v_pk_fma_f32 v[12:13], s[86:87], v[96:97], v[12:13] op_sel:[1,0,0]
	v_pk_fma_f32 v[14:15], s[94:95], v[94:95], v[14:15] op_sel:[1,0,0]
	v_pk_fma_f32 v[16:17], s[94:95], v[96:97], v[16:17] op_sel:[1,0,0]
	s_waitcnt lgkmcnt(0)
	s_load_dwordx8 s[64:71], s[20:21], 0x820
	s_load_dwordx8 s[72:79], s[20:21], 0xa20
	s_load_dwordx8 s[80:87], s[20:21], 0xc20
	s_load_dwordx8 s[88:95], s[20:21], 0xe20
	v_pk_fma_f32 v[18:19], s[32:33], v[34:35], v[18:19] op_sel_hi:[0,1,1]
	v_pk_fma_f32 v[20:21], s[32:33], v[36:37], v[20:21] op_sel_hi:[0,1,1]
	v_pk_fma_f32 v[22:23], s[40:41], v[34:35], v[22:23] op_sel_hi:[0,1,1]
	v_pk_fma_f32 v[24:25], s[40:41], v[36:37], v[24:25] op_sel_hi:[0,1,1]
	v_pk_fma_f32 v[26:27], s[48:49], v[34:35], v[26:27] op_sel_hi:[0,1,1]
	v_pk_fma_f32 v[28:29], s[48:49], v[36:37], v[28:29] op_sel_hi:[0,1,1]
	v_pk_fma_f32 v[30:31], s[56:57], v[34:35], v[30:31] op_sel_hi:[0,1,1]
	v_pk_fma_f32 v[32:33], s[56:57], v[36:37], v[32:33] op_sel_hi:[0,1,1]
	v_pk_fma_f32 v[18:19], s[32:33], v[38:39], v[18:19] op_sel:[1,0,0]
	v_pk_fma_f32 v[20:21], s[32:33], v[40:41], v[20:21] op_sel:[1,0,0]
	v_pk_fma_f32 v[22:23], s[40:41], v[38:39], v[22:23] op_sel:[1,0,0]
	v_pk_fma_f32 v[24:25], s[40:41], v[40:41], v[24:25] op_sel:[1,0,0]
	v_pk_fma_f32 v[26:27], s[48:49], v[38:39], v[26:27] op_sel:[1,0,0]
	v_pk_fma_f32 v[28:29], s[48:49], v[40:41], v[28:29] op_sel:[1,0,0]
	v_pk_fma_f32 v[30:31], s[56:57], v[38:39], v[30:31] op_sel:[1,0,0]
	v_pk_fma_f32 v[32:33], s[56:57], v[40:41], v[32:33] op_sel:[1,0,0]
	v_pk_fma_f32 v[18:19], s[34:35], v[42:43], v[18:19] op_sel_hi:[0,1,1]
	v_pk_fma_f32 v[20:21], s[34:35], v[44:45], v[20:21] op_sel_hi:[0,1,1]
	v_pk_fma_f32 v[22:23], s[42:43], v[42:43], v[22:23] op_sel_hi:[0,1,1]
	v_pk_fma_f32 v[24:25], s[42:43], v[44:45], v[24:25] op_sel_hi:[0,1,1]
	v_pk_fma_f32 v[26:27], s[50:51], v[42:43], v[26:27] op_sel_hi:[0,1,1]
	v_pk_fma_f32 v[28:29], s[50:51], v[44:45], v[28:29] op_sel_hi:[0,1,1]
	v_pk_fma_f32 v[30:31], s[58:59], v[42:43], v[30:31] op_sel_hi:[0,1,1]
	v_pk_fma_f32 v[32:33], s[58:59], v[44:45], v[32:33] op_sel_hi:[0,1,1]
	v_pk_fma_f32 v[18:19], s[34:35], v[46:47], v[18:19] op_sel:[1,0,0]
	v_pk_fma_f32 v[20:21], s[34:35], v[48:49], v[20:21] op_sel:[1,0,0]
	v_pk_fma_f32 v[22:23], s[42:43], v[46:47], v[22:23] op_sel:[1,0,0]
	v_pk_fma_f32 v[24:25], s[42:43], v[48:49], v[24:25] op_sel:[1,0,0]
	v_pk_fma_f32 v[26:27], s[50:51], v[46:47], v[26:27] op_sel:[1,0,0]
	v_pk_fma_f32 v[28:29], s[50:51], v[48:49], v[28:29] op_sel:[1,0,0]
	v_pk_fma_f32 v[30:31], s[58:59], v[46:47], v[30:31] op_sel:[1,0,0]
	v_pk_fma_f32 v[32:33], s[58:59], v[48:49], v[32:33] op_sel:[1,0,0]
	v_pk_fma_f32 v[18:19], s[36:37], v[50:51], v[18:19] op_sel_hi:[0,1,1]
	v_pk_fma_f32 v[20:21], s[36:37], v[52:53], v[20:21] op_sel_hi:[0,1,1]
	v_pk_fma_f32 v[22:23], s[44:45], v[50:51], v[22:23] op_sel_hi:[0,1,1]
	v_pk_fma_f32 v[24:25], s[44:45], v[52:53], v[24:25] op_sel_hi:[0,1,1]
	v_pk_fma_f32 v[26:27], s[52:53], v[50:51], v[26:27] op_sel_hi:[0,1,1]
	v_pk_fma_f32 v[28:29], s[52:53], v[52:53], v[28:29] op_sel_hi:[0,1,1]
	v_pk_fma_f32 v[30:31], s[60:61], v[50:51], v[30:31] op_sel_hi:[0,1,1]
	v_pk_fma_f32 v[32:33], s[60:61], v[52:53], v[32:33] op_sel_hi:[0,1,1]
	v_pk_fma_f32 v[18:19], s[36:37], v[54:55], v[18:19] op_sel:[1,0,0]
	v_pk_fma_f32 v[20:21], s[36:37], v[56:57], v[20:21] op_sel:[1,0,0]
	v_pk_fma_f32 v[22:23], s[44:45], v[54:55], v[22:23] op_sel:[1,0,0]
	v_pk_fma_f32 v[24:25], s[44:45], v[56:57], v[24:25] op_sel:[1,0,0]
	v_pk_fma_f32 v[26:27], s[52:53], v[54:55], v[26:27] op_sel:[1,0,0]
	v_pk_fma_f32 v[28:29], s[52:53], v[56:57], v[28:29] op_sel:[1,0,0]
	v_pk_fma_f32 v[30:31], s[60:61], v[54:55], v[30:31] op_sel:[1,0,0]
	v_pk_fma_f32 v[32:33], s[60:61], v[56:57], v[32:33] op_sel:[1,0,0]
	v_pk_fma_f32 v[18:19], s[38:39], v[58:59], v[18:19] op_sel_hi:[0,1,1]
	v_pk_fma_f32 v[20:21], s[38:39], v[60:61], v[20:21] op_sel_hi:[0,1,1]
	v_pk_fma_f32 v[22:23], s[46:47], v[58:59], v[22:23] op_sel_hi:[0,1,1]
	v_pk_fma_f32 v[24:25], s[46:47], v[60:61], v[24:25] op_sel_hi:[0,1,1]
	v_pk_fma_f32 v[26:27], s[54:55], v[58:59], v[26:27] op_sel_hi:[0,1,1]
	v_pk_fma_f32 v[28:29], s[54:55], v[60:61], v[28:29] op_sel_hi:[0,1,1]
	v_pk_fma_f32 v[30:31], s[62:63], v[58:59], v[30:31] op_sel_hi:[0,1,1]
	v_pk_fma_f32 v[32:33], s[62:63], v[60:61], v[32:33] op_sel_hi:[0,1,1]
	v_pk_fma_f32 v[18:19], s[38:39], v[62:63], v[18:19] op_sel:[1,0,0]
	v_pk_fma_f32 v[20:21], s[38:39], v[64:65], v[20:21] op_sel:[1,0,0]
	v_pk_fma_f32 v[22:23], s[46:47], v[62:63], v[22:23] op_sel:[1,0,0]
	v_pk_fma_f32 v[24:25], s[46:47], v[64:65], v[24:25] op_sel:[1,0,0]
	v_pk_fma_f32 v[26:27], s[54:55], v[62:63], v[26:27] op_sel:[1,0,0]
	v_pk_fma_f32 v[28:29], s[54:55], v[64:65], v[28:29] op_sel:[1,0,0]
	v_pk_fma_f32 v[30:31], s[62:63], v[62:63], v[30:31] op_sel:[1,0,0]
	v_pk_fma_f32 v[32:33], s[62:63], v[64:65], v[32:33] op_sel:[1,0,0]
	s_waitcnt lgkmcnt(0)
	v_pk_fma_f32 v[18:19], s[64:65], v[66:67], v[18:19] op_sel_hi:[0,1,1]
	v_pk_fma_f32 v[20:21], s[64:65], v[68:69], v[20:21] op_sel_hi:[0,1,1]
	v_pk_fma_f32 v[22:23], s[72:73], v[66:67], v[22:23] op_sel_hi:[0,1,1]
	v_pk_fma_f32 v[24:25], s[72:73], v[68:69], v[24:25] op_sel_hi:[0,1,1]
	v_pk_fma_f32 v[26:27], s[80:81], v[66:67], v[26:27] op_sel_hi:[0,1,1]
	v_pk_fma_f32 v[28:29], s[80:81], v[68:69], v[28:29] op_sel_hi:[0,1,1]
	v_pk_fma_f32 v[30:31], s[88:89], v[66:67], v[30:31] op_sel_hi:[0,1,1]
	v_pk_fma_f32 v[32:33], s[88:89], v[68:69], v[32:33] op_sel_hi:[0,1,1]
	v_pk_fma_f32 v[18:19], s[64:65], v[70:71], v[18:19] op_sel:[1,0,0]
	v_pk_fma_f32 v[20:21], s[64:65], v[72:73], v[20:21] op_sel:[1,0,0]
	v_pk_fma_f32 v[22:23], s[72:73], v[70:71], v[22:23] op_sel:[1,0,0]
	v_pk_fma_f32 v[24:25], s[72:73], v[72:73], v[24:25] op_sel:[1,0,0]
	v_pk_fma_f32 v[26:27], s[80:81], v[70:71], v[26:27] op_sel:[1,0,0]
	v_pk_fma_f32 v[28:29], s[80:81], v[72:73], v[28:29] op_sel:[1,0,0]
	v_pk_fma_f32 v[30:31], s[88:89], v[70:71], v[30:31] op_sel:[1,0,0]
	v_pk_fma_f32 v[32:33], s[88:89], v[72:73], v[32:33] op_sel:[1,0,0]
	v_pk_fma_f32 v[18:19], s[66:67], v[74:75], v[18:19] op_sel_hi:[0,1,1]
	v_pk_fma_f32 v[20:21], s[66:67], v[76:77], v[20:21] op_sel_hi:[0,1,1]
	v_pk_fma_f32 v[22:23], s[74:75], v[74:75], v[22:23] op_sel_hi:[0,1,1]
	v_pk_fma_f32 v[24:25], s[74:75], v[76:77], v[24:25] op_sel_hi:[0,1,1]
	v_pk_fma_f32 v[26:27], s[82:83], v[74:75], v[26:27] op_sel_hi:[0,1,1]
	v_pk_fma_f32 v[28:29], s[82:83], v[76:77], v[28:29] op_sel_hi:[0,1,1]
	v_pk_fma_f32 v[30:31], s[90:91], v[74:75], v[30:31] op_sel_hi:[0,1,1]
	v_pk_fma_f32 v[32:33], s[90:91], v[76:77], v[32:33] op_sel_hi:[0,1,1]
	v_pk_fma_f32 v[18:19], s[66:67], v[78:79], v[18:19] op_sel:[1,0,0]
	v_pk_fma_f32 v[20:21], s[66:67], v[80:81], v[20:21] op_sel:[1,0,0]
	v_pk_fma_f32 v[22:23], s[74:75], v[78:79], v[22:23] op_sel:[1,0,0]
	v_pk_fma_f32 v[24:25], s[74:75], v[80:81], v[24:25] op_sel:[1,0,0]
	v_pk_fma_f32 v[26:27], s[82:83], v[78:79], v[26:27] op_sel:[1,0,0]
	v_pk_fma_f32 v[28:29], s[82:83], v[80:81], v[28:29] op_sel:[1,0,0]
	v_pk_fma_f32 v[30:31], s[90:91], v[78:79], v[30:31] op_sel:[1,0,0]
	v_pk_fma_f32 v[32:33], s[90:91], v[80:81], v[32:33] op_sel:[1,0,0]
	v_pk_fma_f32 v[18:19], s[68:69], v[82:83], v[18:19] op_sel_hi:[0,1,1]
	v_pk_fma_f32 v[20:21], s[68:69], v[84:85], v[20:21] op_sel_hi:[0,1,1]
	v_pk_fma_f32 v[22:23], s[76:77], v[82:83], v[22:23] op_sel_hi:[0,1,1]
	v_pk_fma_f32 v[24:25], s[76:77], v[84:85], v[24:25] op_sel_hi:[0,1,1]
	v_pk_fma_f32 v[26:27], s[84:85], v[82:83], v[26:27] op_sel_hi:[0,1,1]
	v_pk_fma_f32 v[28:29], s[84:85], v[84:85], v[28:29] op_sel_hi:[0,1,1]
	v_pk_fma_f32 v[30:31], s[92:93], v[82:83], v[30:31] op_sel_hi:[0,1,1]
	v_pk_fma_f32 v[32:33], s[92:93], v[84:85], v[32:33] op_sel_hi:[0,1,1]
	v_pk_fma_f32 v[18:19], s[68:69], v[86:87], v[18:19] op_sel:[1,0,0]
	v_pk_fma_f32 v[20:21], s[68:69], v[88:89], v[20:21] op_sel:[1,0,0]
	v_pk_fma_f32 v[22:23], s[76:77], v[86:87], v[22:23] op_sel:[1,0,0]
	v_pk_fma_f32 v[24:25], s[76:77], v[88:89], v[24:25] op_sel:[1,0,0]
	v_pk_fma_f32 v[26:27], s[84:85], v[86:87], v[26:27] op_sel:[1,0,0]
	v_pk_fma_f32 v[28:29], s[84:85], v[88:89], v[28:29] op_sel:[1,0,0]
	v_pk_fma_f32 v[30:31], s[92:93], v[86:87], v[30:31] op_sel:[1,0,0]
	v_pk_fma_f32 v[32:33], s[92:93], v[88:89], v[32:33] op_sel:[1,0,0]
	v_pk_fma_f32 v[18:19], s[70:71], v[90:91], v[18:19] op_sel_hi:[0,1,1]
	v_pk_fma_f32 v[20:21], s[70:71], v[92:93], v[20:21] op_sel_hi:[0,1,1]
	v_pk_fma_f32 v[22:23], s[78:79], v[90:91], v[22:23] op_sel_hi:[0,1,1]
	v_pk_fma_f32 v[24:25], s[78:79], v[92:93], v[24:25] op_sel_hi:[0,1,1]
	v_pk_fma_f32 v[26:27], s[86:87], v[90:91], v[26:27] op_sel_hi:[0,1,1]
	v_pk_fma_f32 v[28:29], s[86:87], v[92:93], v[28:29] op_sel_hi:[0,1,1]
	v_pk_fma_f32 v[30:31], s[94:95], v[90:91], v[30:31] op_sel_hi:[0,1,1]
	v_pk_fma_f32 v[32:33], s[94:95], v[92:93], v[32:33] op_sel_hi:[0,1,1]
	v_pk_fma_f32 v[18:19], s[70:71], v[94:95], v[18:19] op_sel:[1,0,0]
	v_pk_fma_f32 v[20:21], s[70:71], v[96:97], v[20:21] op_sel:[1,0,0]
	v_pk_fma_f32 v[22:23], s[78:79], v[94:95], v[22:23] op_sel:[1,0,0]
	v_pk_fma_f32 v[24:25], s[78:79], v[96:97], v[24:25] op_sel:[1,0,0]
	v_pk_fma_f32 v[26:27], s[86:87], v[94:95], v[26:27] op_sel:[1,0,0]
	v_pk_fma_f32 v[28:29], s[86:87], v[96:97], v[28:29] op_sel:[1,0,0]
	v_pk_fma_f32 v[30:31], s[94:95], v[94:95], v[30:31] op_sel:[1,0,0]
	v_pk_fma_f32 v[32:33], s[94:95], v[96:97], v[32:33] op_sel:[1,0,0]
	s_lshl_b32 s9, s23, 13
	v_add_u32_e32 v98, s9, v100
	ds_write_b128 v98, v[2:5] offset:0
	ds_write_b128 v98, v[6:9] offset:1024
	ds_write_b128 v98, v[10:13] offset:2048
	ds_write_b128 v98, v[14:17] offset:3072
	ds_write_b128 v98, v[18:21] offset:4096
	ds_write_b128 v98, v[22:25] offset:5120
	ds_write_b128 v98, v[26:29] offset:6144
	ds_write_b128 v98, v[30:33] offset:7168
	s_lshl_b32 s9, s23, 10
	v_add_u32_e32 v99, s9, v100
	s_waitcnt lgkmcnt(0)
	s_barrier
	ds_read_b128 v[34:37], v99 offset:0
	ds_read_b128 v[38:41], v99 offset:8192
	ds_read_b128 v[42:45], v99 offset:16384
	ds_read_b128 v[46:49], v99 offset:24576
	ds_read_b128 v[50:53], v99 offset:32768
	ds_read_b128 v[54:57], v99 offset:40960
	ds_read_b128 v[58:61], v99 offset:49152
	ds_read_b128 v[62:65], v99 offset:57344
	s_lshl_b32 s8, s27, 3
	s_add_u32 s8, s8, s23
	s_lshl_b32 s8, s8, 11
	s_lshl_b32 s9, s30, 10
	s_add_u32 s8, s8, s9
	s_add_u32 s28, s28, s8
	s_addc_u32 s29, s29, 0
	s_waitcnt lgkmcnt(6)
	v_pk_add_f32 v[34:35], v[34:35], v[38:39]
	v_pk_add_f32 v[36:37], v[36:37], v[40:41]
	s_waitcnt lgkmcnt(5)
	v_pk_add_f32 v[34:35], v[34:35], v[42:43]
	v_pk_add_f32 v[36:37], v[36:37], v[44:45]
	s_waitcnt lgkmcnt(4)
	v_pk_add_f32 v[34:35], v[34:35], v[46:47]
	v_pk_add_f32 v[36:37], v[36:37], v[48:49]
	s_waitcnt lgkmcnt(3)
	v_pk_add_f32 v[34:35], v[34:35], v[50:51]
	v_pk_add_f32 v[36:37], v[36:37], v[52:53]
	s_waitcnt lgkmcnt(2)
	v_pk_add_f32 v[34:35], v[34:35], v[54:55]
	v_pk_add_f32 v[36:37], v[36:37], v[56:57]
	s_waitcnt lgkmcnt(1)
	v_pk_add_f32 v[34:35], v[34:35], v[58:59]
	v_pk_add_f32 v[36:37], v[36:37], v[60:61]
	s_waitcnt lgkmcnt(0)
	v_pk_add_f32 v[34:35], v[34:35], v[62:63]
	v_pk_add_f32 v[36:37], v[36:37], v[64:65]
	global_store_dwordx4 v100, v[34:37], s[28:29] sc0 sc1

.LBB0_8:
	s_and_b64 vcc, exec, s[4:5]
	s_cbranch_vccz .LBB0_10
	s_load_dwordx4 s[4:7], s[0:1], 0x10
	s_lshl_b32 s3, s2, 9
	v_or_b32_e32 v1, s3, v0
	v_lshrrev_b32_e32 v2, 6, v1
	v_lshlrev_b32_e32 v2, 9, v2
	v_mov_b32_e32 v3, 0
	s_waitcnt lgkmcnt(0)
	v_lshl_add_u64 v[4:5], v[2:3], 2, s[4:5]
	v_lshlrev_b32_e32 v2, 5, v0
	v_and_b32_e32 v2, 0x7e0, v2
	v_lshl_add_u64 v[10:11], v[4:5], 0, v[2:3]
	global_load_dwordx4 v[2:5], v[10:11], off
	global_load_dwordx4 v[6:9], v[10:11], off offset:16
	v_lshlrev_b32_e32 v11, 1, v0
	s_lshr_b32 s5, s2, 1
	v_and_b32_e32 v11, 0x78, v11
	v_lshlrev_b32_e32 v10, 4, v0
	v_mov_b32_e32 v12, 0xe000
	v_bfe_u32 v1, v1, 6, 4
	v_and_or_b32 v11, s5, 7, v11
	s_brev_b32 s4, 34
	v_bitop3_b32 v12, s3, v12, v0 bitop3:0xc8
	v_and_or_b32 v1, v10, 48, v1
	v_lshlrev_b32_e32 v10, 6, v11
	v_or3_b32 v1, v10, v12, v1
	v_lshlrev_b32_e32 v1, 4, v1
	s_waitcnt vmcnt(1)
	v_pk_mul_f32 v[2:3], v[2:3], s[4:5] op_sel_hi:[1,0]
	v_pk_mul_f32 v[4:5], v[4:5], s[4:5] op_sel_hi:[1,0]
	s_waitcnt vmcnt(0)
	v_pk_mul_f32 v[6:7], v[6:7], s[4:5] op_sel_hi:[1,0]
	v_pk_mul_f32 v[8:9], v[8:9], s[4:5] op_sel_hi:[1,0]
	v_cvt_pk_f16_f32 v2, v2, v3
	v_cvt_pk_f16_f32 v3, v4, v5
	v_cvt_pk_f16_f32 v4, v6, v7
	v_cvt_pk_f16_f32 v5, v8, v9
	global_store_dwordx4 v1, v[2:5], s[6:7] sc0 sc1

.LBB0_51:
	s_andn2_b64 vcc, exec, s[4:5]
	s_cbranch_vccnz .LBB0_54
	v_lshl_or_b32 v1, s2, 9, v0
	v_add_u32_e32 v2, 0xfffe7e00, v1
	s_movk_i32 s2, 0x4000
	v_cmp_gt_i32_e32 vcc, s2, v2
	s_and_saveexec_b64 s[2:3], vcc
	s_cbranch_execz .LBB0_54
	s_load_dwordx4 s[4:7], s[0:1], 0x30
	v_lshrrev_b32_e32 v3, 1, v0
	v_lshrrev_b32_e32 v1, 1, v2
	v_and_b32_e32 v3, 24, v3
	s_movk_i32 s0, 0x1e0
	v_and_or_b32 v1, v1, s0, v3
	v_lshlrev_b32_e32 v4, 10, v1
	v_ashrrev_i32_e32 v1, 6, v2
	v_mov_b32_e32 v5, 0
	v_and_b32_e32 v8, -16, v1
	s_waitcnt lgkmcnt(0)
	v_lshl_add_u64 v[6:7], s[4:5], 0, v[4:5]
	v_ashrrev_i32_e32 v9, 31, v8
	v_and_b32_e32 v0, 15, v0
	v_lshl_add_u64 v[6:7], v[8:9], 2, v[6:7]
	v_lshlrev_b32_e32 v4, 2, v0
	v_lshl_add_u64 v[0:1], v[6:7], 0, v[4:5]
	s_movk_i32 s0, 0x1000
	v_add_co_u32_e32 v4, vcc, s0, v0
	v_ashrrev_i32_e32 v3, 31, v2
	s_nop 0
	v_addc_co_u32_e32 v5, vcc, 0, v1, vcc
	global_load_dword v6, v[0:1], off
	global_load_dword v7, v[0:1], off offset:1024
	global_load_dword v8, v[0:1], off offset:2048
	global_load_dword v9, v[0:1], off offset:3072
	global_load_dword v10, v[4:5], off
	global_load_dword v11, v[4:5], off offset:2048
	global_load_dword v12, v[4:5], off offset:3072
	global_load_dword v13, v[4:5], off offset:1024
	v_lshl_add_u64 v[0:1], v[2:3], 4, s[6:7]
	s_waitcnt vmcnt(6)
	v_cvt_pk_f16_f32 v4, v6, v7
	s_waitcnt vmcnt(4)
	v_cvt_pk_f16_f32 v5, v8, v9
	s_waitcnt vmcnt(1)
	v_cvt_pk_f16_f32 v7, v11, v12
	s_waitcnt vmcnt(0)
	v_cvt_pk_f16_f32 v6, v10, v13
	global_store_dwordx4 v[0:1], v[4:7], off sc0 sc1
